# refine results published as 8-byte {value,tag} granules (one sc1 store, no fence/counter); selection polls granules directly
# speedup vs baseline: 1.0205x; 1.0018x over previous
.LBB2_18:
	s_or_b64 exec, exec, s[30:31]
	s_waitcnt lgkmcnt(0)
	s_barrier
	s_and_saveexec_b64 s[30:31], s[6:7]
	s_cbranch_execz .LBB2_5
	ds_read_b128 v[14:17], v1 offset:16384
	s_or_b32 s28, s39, s37
	s_lshl_b64 s[42:43], s[28:29], 8
	s_add_u32 s42, s16, s42
	s_addc_u32 s43, s17, s43
	s_sub_u32 s42, s42, 0x104000
	s_subb_u32 s43, s43, 0
	s_waitcnt lgkmcnt(0)
	v_add_f32_e32 v14, v14, v15
	v_add_f32_e32 v14, v14, v16
	s_lshl_b32 s28, s36, 3
	v_add_f32_e32 v14, v14, v17
	v_mov_b32_e32 v16, s28
	v_mov_b32_e32 v15, -1
	global_store_dwordx2 v16, v[14:15], s[42:43] sc1
	s_branch .LBB2_5
.LBB2_21:
.LBB2_26:
	s_load_dwordx2 s[6:7], s[0:1], 0x48
	s_ashr_i32 s0, s2, 3
	s_and_b32 s0, s0, -8
	s_and_b32 s1, s2, 6
	s_or_b32 s0, s0, s1
	s_ashr_i32 s8, s0, 1
	s_and_saveexec_b64 s[18:19], s[10:11]
	s_cbranch_execz .LBB2_160
	v_mov_b32_e32 v1, 0
	ds_read_b64 v[2:3], v1 offset:16400
	v_lshlrev_b64 v[4:5], v26, 1
	s_andn2_b64 vcc, exec, s[4:5]
	s_waitcnt lgkmcnt(0)
	v_and_b32_e32 v7, v3, v5
	v_and_b32_e32 v6, v2, v4
	v_cmp_ne_u64_e64 s[10:11], 0, v[6:7]
	s_cbranch_vccnz .LBB2_157
	v_and_b32_e32 v5, s25, v5
	v_and_b32_e32 v4, s24, v4
	v_cmp_ne_u64_e64 s[4:5], 0, v[4:5]
	s_mov_b64 s[0:1], exec
	s_nop 0
	v_writelane_b32 v86, s4, 0
	s_nop 1
	v_writelane_b32 v86, s5, 1
	s_and_b64 s[4:5], s[0:1], s[4:5]
	s_mov_b64 exec, s[4:5]
	s_cbranch_execz .LBB2_30
	v_lshlrev_b32_e32 v1, 8, v0
	v_lshl_or_b32 v1, s3, 14, v1
	s_sub_u32 s16, s16, 0x104000
	s_subb_u32 s17, s17, 0
.Lrg_gpoll:
	global_load_dwordx2 v[104:105], v1, s[16:17] offset:0 sc1
	global_load_dwordx2 v[106:107], v1, s[16:17] offset:8 sc1
	global_load_dwordx2 v[108:109], v1, s[16:17] offset:16 sc1
	global_load_dwordx2 v[110:111], v1, s[16:17] offset:24 sc1
	global_load_dwordx2 v[112:113], v1, s[16:17] offset:32 sc1
	global_load_dwordx2 v[114:115], v1, s[16:17] offset:40 sc1
	global_load_dwordx2 v[116:117], v1, s[16:17] offset:48 sc1
	global_load_dwordx2 v[118:119], v1, s[16:17] offset:56 sc1
	global_load_dwordx2 v[120:121], v1, s[16:17] offset:64 sc1
	global_load_dwordx2 v[122:123], v1, s[16:17] offset:72 sc1
	global_load_dwordx2 v[124:125], v1, s[16:17] offset:80 sc1
	global_load_dwordx2 v[126:127], v1, s[16:17] offset:88 sc1
	global_load_dwordx2 v[128:129], v1, s[16:17] offset:96 sc1
	global_load_dwordx2 v[130:131], v1, s[16:17] offset:104 sc1
	global_load_dwordx2 v[132:133], v1, s[16:17] offset:112 sc1
	global_load_dwordx2 v[134:135], v1, s[16:17] offset:120 sc1
	global_load_dwordx2 v[136:137], v1, s[16:17] offset:128 sc1
	global_load_dwordx2 v[138:139], v1, s[16:17] offset:136 sc1
	global_load_dwordx2 v[140:141], v1, s[16:17] offset:144 sc1
	global_load_dwordx2 v[142:143], v1, s[16:17] offset:152 sc1
	global_load_dwordx2 v[144:145], v1, s[16:17] offset:160 sc1
	global_load_dwordx2 v[146:147], v1, s[16:17] offset:168 sc1
	global_load_dwordx2 v[148:149], v1, s[16:17] offset:176 sc1
	global_load_dwordx2 v[150:151], v1, s[16:17] offset:184 sc1
	global_load_dwordx2 v[152:153], v1, s[16:17] offset:192 sc1
	global_load_dwordx2 v[154:155], v1, s[16:17] offset:200 sc1
	global_load_dwordx2 v[156:157], v1, s[16:17] offset:208 sc1
	global_load_dwordx2 v[158:159], v1, s[16:17] offset:216 sc1
	global_load_dwordx2 v[160:161], v1, s[16:17] offset:224 sc1
	global_load_dwordx2 v[162:163], v1, s[16:17] offset:232 sc1
	global_load_dwordx2 v[164:165], v1, s[16:17] offset:240 sc1
	global_load_dwordx2 v[166:167], v1, s[16:17] offset:248 sc1
	s_waitcnt vmcnt(0)
	v_and_b32_e32 v4, v105, v107
	v_and_b32_e32 v4, v4, v109
	v_and_b32_e32 v4, v4, v111
	v_and_b32_e32 v4, v4, v113
	v_and_b32_e32 v4, v4, v115
	v_and_b32_e32 v4, v4, v117
	v_and_b32_e32 v4, v4, v119
	v_and_b32_e32 v4, v4, v121
	v_and_b32_e32 v4, v4, v123
	v_and_b32_e32 v4, v4, v125
	v_and_b32_e32 v4, v4, v127
	v_and_b32_e32 v4, v4, v129
	v_and_b32_e32 v4, v4, v131
	v_and_b32_e32 v4, v4, v133
	v_and_b32_e32 v4, v4, v135
	v_and_b32_e32 v4, v4, v137
	v_and_b32_e32 v4, v4, v139
	v_and_b32_e32 v4, v4, v141
	v_and_b32_e32 v4, v4, v143
	v_and_b32_e32 v4, v4, v145
	v_and_b32_e32 v4, v4, v147
	v_and_b32_e32 v4, v4, v149
	v_and_b32_e32 v4, v4, v151
	v_and_b32_e32 v4, v4, v153
	v_and_b32_e32 v4, v4, v155
	v_and_b32_e32 v4, v4, v157
	v_and_b32_e32 v4, v4, v159
	v_and_b32_e32 v4, v4, v161
	v_and_b32_e32 v4, v4, v163
	v_and_b32_e32 v4, v4, v165
	v_and_b32_e32 v4, v4, v167
	v_cmp_ne_u32_e32 vcc, -1, v4
	s_cbranch_vccz .Lrg_gdone
	s_sleep 8
	s_branch .Lrg_gpoll
.Lrg_gdone:
	v_add_f32_e32 v1, 0, v104
	v_add_f32_e32 v1, v1, v106
	v_add_f32_e32 v1, v1, v108
	v_add_f32_e32 v1, v1, v110
	v_add_f32_e32 v1, v1, v112
	v_add_f32_e32 v1, v1, v114
	v_add_f32_e32 v1, v1, v116
	v_add_f32_e32 v1, v1, v118
	v_add_f32_e32 v1, v1, v120
	v_add_f32_e32 v1, v1, v122
	v_add_f32_e32 v1, v1, v124
	v_add_f32_e32 v1, v1, v126
	v_add_f32_e32 v1, v1, v128
	v_add_f32_e32 v1, v1, v130
	v_add_f32_e32 v1, v1, v132
	v_add_f32_e32 v1, v1, v134
	v_add_f32_e32 v1, v1, v136
	v_add_f32_e32 v1, v1, v138
	v_add_f32_e32 v1, v1, v140
	v_add_f32_e32 v1, v1, v142
	v_add_f32_e32 v1, v1, v144
	v_add_f32_e32 v1, v1, v146
	v_add_f32_e32 v1, v1, v148
	v_add_f32_e32 v1, v1, v150
	v_add_f32_e32 v1, v1, v152
	v_add_f32_e32 v1, v1, v154
	v_add_f32_e32 v1, v1, v156
	v_add_f32_e32 v1, v1, v158
	v_add_f32_e32 v1, v1, v160
	v_add_f32_e32 v1, v1, v162
	v_add_f32_e32 v1, v1, v164
	v_add_f32_e32 v1, v1, v166
	v_mov_b32_e32 v4, s33
	v_fmamk_f32 v1, v1, 0x3c800000, v4
